# speedup vs baseline: 1.0473x; 1.0066x over previous
.LBB3_47:
	s_nop 0
	v_lshlrev_b32_e32 v10, 19, v8
	s_and_b32 s8, s6, 0x300
	s_add_i32 s9, s6, 0x100
	v_add_u32_e32 v10, 0xe0000000, v10
	s_bfe_i32 s0, s7, 0x10003
	s_and_b32 s1, s6, 0x200
	v_bfe_i32 v11, v8, 12, 1
	v_add_u32_e32 v12, s6, v9
	v_or_b32_e32 v14, s8, v7
	s_and_b32 s8, s9, 0x300
	v_ashrrev_i32_e32 v10, 31, v10
	s_and_b32 s10, s0, 0x13700
	v_or_b32_e32 v13, s1, v148
	v_and_b32_e32 v11, 0x13700, v11
	v_and_or_b32 v12, v12, s5, v7
	v_or_b32_e32 v15, s8, v148
	v_and_b32_e32 v16, 0x13700, v10
	v_lshl_add_u32 v13, v13, 6, s10
	v_lshl_add_u32 v11, v12, 6, v11
	v_lshl_add_u32 v15, v15, 6, s10
	v_lshl_add_u32 v18, v14, 6, v16
	v_or_b32_e32 v12, v13, v6
	v_or_b32_e32 v17, v11, v6
	v_or_b32_e32 v19, v15, v6
	v_or_b32_e32 v22, v18, v6
	ds_read_b128 v[10:13], v12
	ds_read_b128 v[14:17], v17
	ds_read_b128 v[18:21], v19
	ds_read_b128 v[22:25], v22
	s_add_i32 s7, s7, 4
	v_lshl_add_u64 v[30:31], v[4:5], 0, s[2:3]
	v_lshl_add_u64 v[32:33], v[0:1], 0, s[2:3]
	v_lshl_add_u64 v[34:35], v[2:3], 0, s[2:3]
	s_add_u32 s2, s2, 0x40c000
	s_addc_u32 s3, s3, 0
	s_addk_i32 s6, 0x200
	v_add_u32_e32 v8, 0x800, v8
	v_add_co_u32_e64 v36, s[0:1], s4, v30
	s_cmp_eq_u32 s2, 0x1030000
	s_waitcnt lgkmcnt(3)
	v_cndmask_b32_e32 v27, v13, v11, vcc
	v_cndmask_b32_e32 v26, v12, v10, vcc
	v_cndmask_b32_e32 v29, v11, v13, vcc
	v_cndmask_b32_e32 v28, v10, v12, vcc
	s_waitcnt lgkmcnt(2)
	v_cndmask_b32_e32 v11, v17, v15, vcc
	v_cndmask_b32_e32 v10, v16, v14, vcc
	v_cndmask_b32_e32 v13, v15, v17, vcc
	v_cndmask_b32_e32 v12, v14, v16, vcc
	s_waitcnt lgkmcnt(1)
	v_cndmask_b32_e32 v15, v21, v19, vcc
	v_cndmask_b32_e32 v14, v20, v18, vcc
	v_cndmask_b32_e32 v17, v19, v21, vcc
	v_cndmask_b32_e32 v16, v18, v20, vcc
	s_waitcnt lgkmcnt(0)
	v_cndmask_b32_e32 v19, v25, v23, vcc
	v_cndmask_b32_e32 v18, v24, v22, vcc
	v_cndmask_b32_e32 v21, v23, v25, vcc
	v_cndmask_b32_e32 v20, v22, v24, vcc
	v_addc_co_u32_e64 v37, s[0:1], 0, v31, s[0:1]
	global_store_dwordx4 v[30:31], v[26:29], off sc1
	global_store_dwordx4 v[32:33], v[18:21], off sc1
	global_store_dwordx4 v[36:37], v[14:17], off sc1
	global_store_dwordx4 v[34:35], v[10:13], off sc1
	s_cbranch_scc0 .LBB3_47
	s_endpgm

.LBB7_38:
	s_or_b64 exec, exec, s[0:1]
	s_lshl_b64 s[0:1], s[6:7], 2
	s_waitcnt lgkmcnt(0)
	s_add_u32 s4, s8, s0
	s_addc_u32 s5, s9, s1
	s_lshl_b32 s10, s6, 12
	s_waitcnt vmcnt(0)
	v_cmp_ne_u32_e32 vcc, 0, v15
	v_lshrrev_b32_e32 v17, 19, v15
	v_cmp_ge_i32_e64 s[12:13], v17, v16
	s_and_b64 s[20:21], vcc, s[12:13]
	s_bcnt1_i32_b64 s40, s[20:21]
	v_cmp_ne_u32_e32 vcc, 0, v13
	v_lshrrev_b32_e32 v17, 19, v13
	v_cmp_ge_i32_e64 s[12:13], v17, v16
	s_and_b64 s[22:23], vcc, s[12:13]
	s_bcnt1_i32_b64 s41, s[22:23]
	v_cmp_ne_u32_e32 vcc, 0, v11
	v_lshrrev_b32_e32 v17, 19, v11
	v_cmp_ge_i32_e64 s[12:13], v17, v16
	s_and_b64 s[24:25], vcc, s[12:13]
	s_bcnt1_i32_b64 s42, s[24:25]
	v_cmp_ne_u32_e32 vcc, 0, v9
	v_lshrrev_b32_e32 v17, 19, v9
	v_cmp_ge_i32_e64 s[12:13], v17, v16
	s_and_b64 s[26:27], vcc, s[12:13]
	s_bcnt1_i32_b64 s43, s[26:27]
	v_cmp_ne_u32_e32 vcc, 0, v7
	v_lshrrev_b32_e32 v17, 19, v7
	v_cmp_ge_i32_e64 s[12:13], v17, v16
	s_and_b64 s[28:29], vcc, s[12:13]
	s_bcnt1_i32_b64 s44, s[28:29]
	v_cmp_ne_u32_e32 vcc, 0, v5
	v_lshrrev_b32_e32 v17, 19, v5
	v_cmp_ge_i32_e64 s[12:13], v17, v16
	s_and_b64 s[30:31], vcc, s[12:13]
	s_bcnt1_i32_b64 s45, s[30:31]
	v_cmp_ne_u32_e32 vcc, 0, v3
	v_lshrrev_b32_e32 v17, 19, v3
	v_cmp_ge_i32_e64 s[12:13], v17, v16
	s_and_b64 s[32:33], vcc, s[12:13]
	s_bcnt1_i32_b64 s46, s[32:33]
	v_cmp_ne_u32_e32 vcc, 0, v1
	v_lshrrev_b32_e32 v17, 19, v1
	v_cmp_ge_i32_e64 s[12:13], v17, v16
	s_and_b64 s[34:35], vcc, s[12:13]
	s_bcnt1_i32_b64 s47, s[34:35]
	s_add_i32 s11, s40, s41
	s_add_i32 s11, s11, s42
	s_add_i32 s11, s11, s43
	s_add_i32 s11, s11, s44
	s_add_i32 s11, s11, s45
	s_add_i32 s11, s11, s46
	s_add_i32 s11, s11, s47
	s_cmp_eq_u32 s11, 0
	s_cbranch_scc1 .Lmy_collect_done
	v_mov_b32_e32 v17, 0
	v_mov_b32_e32 v18, s11
	s_mov_b64 exec, 1
	global_atomic_add v17, v17, v18, s[4:5] sc0
	s_mov_b64 exec, -1
	s_movk_i32 s15, 0x1000
	s_waitcnt vmcnt(0)
	v_readfirstlane_b32 s14, v17
	v_mbcnt_lo_u32_b32 v19, s20, 0
	v_mbcnt_hi_u32_b32 v19, s21, v19
	v_add_u32_e32 v19, s14, v19
	v_cmp_gt_i32_e32 vcc, s15, v19
	v_add_lshl_u32 v20, v19, s10, 2
	s_and_b64 exec, s[20:21], vcc
	global_store_dword v20, v14, s[2:3]
	s_mov_b64 exec, -1
	s_add_i32 s14, s14, s40
	v_mbcnt_lo_u32_b32 v19, s22, 0
	v_mbcnt_hi_u32_b32 v19, s23, v19
	v_add_u32_e32 v19, s14, v19
	v_cmp_gt_i32_e32 vcc, s15, v19
	v_add_lshl_u32 v20, v19, s10, 2
	s_and_b64 exec, s[22:23], vcc
	global_store_dword v20, v12, s[2:3]
	s_mov_b64 exec, -1
	s_add_i32 s14, s14, s41
	v_mbcnt_lo_u32_b32 v19, s24, 0
	v_mbcnt_hi_u32_b32 v19, s25, v19
	v_add_u32_e32 v19, s14, v19
	v_cmp_gt_i32_e32 vcc, s15, v19
	v_add_lshl_u32 v20, v19, s10, 2
	s_and_b64 exec, s[24:25], vcc
	global_store_dword v20, v10, s[2:3]
	s_mov_b64 exec, -1
	s_add_i32 s14, s14, s42
	v_mbcnt_lo_u32_b32 v19, s26, 0
	v_mbcnt_hi_u32_b32 v19, s27, v19
	v_add_u32_e32 v19, s14, v19
	v_cmp_gt_i32_e32 vcc, s15, v19
	v_add_lshl_u32 v20, v19, s10, 2
	s_and_b64 exec, s[26:27], vcc
	global_store_dword v20, v8, s[2:3]
	s_mov_b64 exec, -1
	s_add_i32 s14, s14, s43
	v_mbcnt_lo_u32_b32 v19, s28, 0
	v_mbcnt_hi_u32_b32 v19, s29, v19
	v_add_u32_e32 v19, s14, v19
	v_cmp_gt_i32_e32 vcc, s15, v19
	v_add_lshl_u32 v20, v19, s10, 2
	s_and_b64 exec, s[28:29], vcc
	global_store_dword v20, v6, s[2:3]
	s_mov_b64 exec, -1
	s_add_i32 s14, s14, s44
	v_mbcnt_lo_u32_b32 v19, s30, 0
	v_mbcnt_hi_u32_b32 v19, s31, v19
	v_add_u32_e32 v19, s14, v19
	v_cmp_gt_i32_e32 vcc, s15, v19
	v_add_lshl_u32 v20, v19, s10, 2
	s_and_b64 exec, s[30:31], vcc
	global_store_dword v20, v4, s[2:3]
	s_mov_b64 exec, -1
	s_add_i32 s14, s14, s45
	v_mbcnt_lo_u32_b32 v19, s32, 0
	v_mbcnt_hi_u32_b32 v19, s33, v19
	v_add_u32_e32 v19, s14, v19
	v_cmp_gt_i32_e32 vcc, s15, v19
	v_add_lshl_u32 v20, v19, s10, 2
	s_and_b64 exec, s[32:33], vcc
	global_store_dword v20, v2, s[2:3]
	s_mov_b64 exec, -1
	s_add_i32 s14, s14, s46
	v_mbcnt_lo_u32_b32 v19, s34, 0
	v_mbcnt_hi_u32_b32 v19, s35, v19
	v_add_u32_e32 v19, s14, v19
	v_cmp_gt_i32_e32 vcc, s15, v19
	v_add_lshl_u32 v20, v19, s10, 2
	s_and_b64 exec, s[34:35], vcc
	global_store_dword v20, v0, s[2:3]
	s_mov_b64 exec, -1
	s_add_i32 s14, s14, s47

	.amdhsa_kernel _Z14collect_kernelPKjS0_PiS1_
		.amdhsa_group_segment_fixed_size 2052
		.amdhsa_private_segment_fixed_size 0
		.amdhsa_kernarg_size 32
		.amdhsa_user_sgpr_count 2
		.amdhsa_user_sgpr_dispatch_ptr 0
		.amdhsa_user_sgpr_queue_ptr 0
		.amdhsa_user_sgpr_kernarg_segment_ptr 1
		.amdhsa_user_sgpr_dispatch_id 0
		.amdhsa_user_sgpr_kernarg_preload_length 0
		.amdhsa_user_sgpr_kernarg_preload_offset 0
		.amdhsa_user_sgpr_private_segment_size 0
		.amdhsa_uses_dynamic_stack 0
		.amdhsa_enable_private_segment 0
		.amdhsa_system_sgpr_workgroup_id_x 1
		.amdhsa_system_sgpr_workgroup_id_y 1
		.amdhsa_system_sgpr_workgroup_id_z 0
		.amdhsa_system_sgpr_workgroup_info 0
		.amdhsa_system_vgpr_workitem_id 0
		.amdhsa_next_free_vgpr 34
		.amdhsa_next_free_sgpr 48
		.amdhsa_accum_offset 36
		.amdhsa_reserve_vcc 1
		.amdhsa_float_round_mode_32 0
		.amdhsa_float_round_mode_16_64 0
		.amdhsa_float_denorm_mode_32 3
		.amdhsa_float_denorm_mode_16_64 3
		.amdhsa_dx10_clamp 1
		.amdhsa_ieee_mode 1
		.amdhsa_fp16_overflow 0
		.amdhsa_tg_split 0
		.amdhsa_exception_fp_ieee_invalid_op 0
		.amdhsa_exception_fp_denorm_src 0
		.amdhsa_exception_fp_ieee_div_zero 0
		.amdhsa_exception_fp_ieee_overflow 0
		.amdhsa_exception_fp_ieee_underflow 0
		.amdhsa_exception_fp_ieee_inexact 0
		.amdhsa_exception_int_div_zero 0
	.end_amdhsa_kernel

.LBB15_32:
	ds_read_b128 v[10:13], v7
	ds_read_b128 v[14:17], v6
	ds_read_b128 v[18:21], v6 offset:16384
	ds_read_b128 v[30:33], v8
	v_lshl_add_u64 v[22:23], v[2:3], 0, s[6:7]
	v_lshl_add_u64 v[38:39], v[4:5], 0, s[6:7]
	v_lshl_add_u64 v[40:41], v[0:1], 0, s[6:7]
	s_add_u32 s6, s6, 0x40c000
	s_addc_u32 s7, s7, 0
	v_add_u32_e32 v8, 0x8000, v8
	v_add_u32_e32 v7, 0x8000, v7
	v_add_u32_e32 v6, 0x8000, v6
	v_add_co_u32_e32 v42, vcc, s13, v22
	s_cmp_eq_u32 s6, 0x818000
	s_waitcnt lgkmcnt(2)
	v_cndmask_b32_e64 v35, v17, v15, s[0:1]
	v_cndmask_b32_e64 v34, v16, v14, s[0:1]
	v_cndmask_b32_e64 v37, v15, v17, s[0:1]
	v_cndmask_b32_e64 v36, v14, v16, s[0:1]
	v_addc_co_u32_e32 v43, vcc, 0, v23, vcc
	v_cndmask_b32_e64 v15, v13, v11, s[0:1]
	v_cndmask_b32_e64 v14, v12, v10, s[0:1]
	v_cndmask_b32_e64 v17, v11, v13, s[0:1]
	v_cndmask_b32_e64 v16, v10, v12, s[0:1]
	s_waitcnt lgkmcnt(1)
	v_cndmask_b32_e64 v11, v21, v19, s[0:1]
	v_cndmask_b32_e64 v10, v20, v18, s[0:1]
	v_cndmask_b32_e64 v13, v19, v21, s[0:1]
	v_cndmask_b32_e64 v12, v18, v20, s[0:1]
	s_waitcnt lgkmcnt(0)
	v_cndmask_b32_e64 v19, v33, v31, s[0:1]
	v_cndmask_b32_e64 v18, v32, v30, s[0:1]
	v_cndmask_b32_e64 v21, v31, v33, s[0:1]
	v_cndmask_b32_e64 v20, v30, v32, s[0:1]
	global_store_dwordx4 v[22:23], v[34:37], off sc1
	global_store_dwordx4 v[38:39], v[14:17], off sc1
	global_store_dwordx4 v[42:43], v[10:13], off sc1
	global_store_dwordx4 v[40:41], v[18:21], off sc1
	s_cbranch_scc0 .LBB15_32
	s_mov_b32 s11, 1
	s_mov_b64 s[6:7], 0
	s_and_b64 vcc, exec, s[8:9]
	s_barrier
	s_cbranch_vccz .LBB15_29
	s_endpgm

amdhsa.kernels:
  - .agpr_count:     0
    .args:
      - .actual_access:  read_only
        .address_space:  global
        .offset:         0
        .size:           8
        .value_kind:     global_buffer
      - .actual_access:  write_only
        .address_space:  global
        .offset:         8
        .size:           8
        .value_kind:     global_buffer
    .group_segment_fixed_size: 0
    .kernarg_segment_align: 8
    .kernarg_segment_size: 16
    .language:       OpenCL C
    .language_version:
      - 2
      - 0
    .max_flat_workgroup_size: 256
    .name:           _Z13prep_x_kernelPKfP15HIP_vector_typeIjLj4EE
    .private_segment_fixed_size: 0
    .sgpr_count:     23
    .sgpr_spill_count: 0
    .symbol:         _Z13prep_x_kernelPKfP15HIP_vector_typeIjLj4EE.kd
    .uniform_work_group_size: 1
    .uses_dynamic_stack: false
    .vgpr_count:     36
    .vgpr_spill_count: 0
    .wavefront_size: 64
  - .agpr_count:     0
    .args:
      - .actual_access:  read_only
        .address_space:  global
        .offset:         0
        .size:           8
        .value_kind:     global_buffer
      - .actual_access:  write_only
        .address_space:  global
        .offset:         8
        .size:           8
        .value_kind:     global_buffer
      - .offset:         16
        .size:           4
        .value_kind:     by_value
      - .offset:         20
        .size:           4
        .value_kind:     by_value
      - .offset:         24
        .size:           4
        .value_kind:     by_value
      - .offset:         28
        .size:           4
        .value_kind:     by_value
    .group_segment_fixed_size: 0
    .kernarg_segment_align: 8
    .kernarg_segment_size: 32
    .language:       OpenCL C
    .language_version:
      - 2
      - 0
    .max_flat_workgroup_size: 256
    .name:           _Z13prep_w_kernelPKfP15HIP_vector_typeIjLj4EEiiii
    .private_segment_fixed_size: 0
    .sgpr_count:     15
    .sgpr_spill_count: 0
    .symbol:         _Z13prep_w_kernelPKfP15HIP_vector_typeIjLj4EEiiii.kd
    .uniform_work_group_size: 1
    .uses_dynamic_stack: false
    .vgpr_count:     34
    .vgpr_spill_count: 0
    .wavefront_size: 64
  - .agpr_count:     0
    .args:
      - .actual_access:  write_only
        .address_space:  global
        .offset:         0
        .size:           8
        .value_kind:     global_buffer
    .group_segment_fixed_size: 0
    .kernarg_segment_align: 8
    .kernarg_segment_size: 8
    .language:       OpenCL C
    .language_version:
      - 2
      - 0
    .max_flat_workgroup_size: 256
    .name:           _Z18zero_border_kernelP15HIP_vector_typeIjLj4EE
    .private_segment_fixed_size: 0
    .sgpr_count:     12
    .sgpr_spill_count: 0
    .symbol:         _Z18zero_border_kernelP15HIP_vector_typeIjLj4EE.kd
    .uniform_work_group_size: 1
    .uses_dynamic_stack: false
    .vgpr_count:     6
    .vgpr_spill_count: 0
    .wavefront_size: 64
  - .agpr_count:     0
    .args:
      - .actual_access:  read_only
        .address_space:  global
        .offset:         0
        .size:           8
        .value_kind:     global_buffer
      - .address_space:  global
        .offset:         8
        .size:           8
        .value_kind:     global_buffer
      - .actual_access:  read_only
        .address_space:  global
        .offset:         16
        .size:           8
        .value_kind:     global_buffer
      - .actual_access:  read_only
        .address_space:  global
        .offset:         24
        .size:           8
        .value_kind:     global_buffer
      - .actual_access:  read_only
        .address_space:  global
        .offset:         32
        .size:           8
        .value_kind:     global_buffer
      - .actual_access:  write_only
        .address_space:  global
        .offset:         40
        .size:           8
        .value_kind:     global_buffer
    .group_segment_fixed_size: 154880
    .kernarg_segment_align: 8
    .kernarg_segment_size: 48
    .language:       OpenCL C
    .language_version:
      - 2
      - 0
    .max_flat_workgroup_size: 512
    .name:           _Z12conv1_kernelPKfPK15HIP_vector_typeIjLj4EES0_S0_S0_PDF16_
    .private_segment_fixed_size: 0
    .sgpr_count:     46
    .sgpr_spill_count: 0
    .symbol:         _Z12conv1_kernelPKfPK15HIP_vector_typeIjLj4EES0_S0_S0_PDF16_.kd
    .uniform_work_group_size: 1
    .uses_dynamic_stack: false
    .vgpr_count:     256
    .vgpr_spill_count: 0
    .wavefront_size: 64
  - .agpr_count:     0
    .args:
      - .actual_access:  read_only
        .address_space:  global
        .offset:         0
        .size:           8
        .value_kind:     global_buffer
      - .actual_access:  read_only
        .address_space:  global
        .offset:         8
        .size:           8
        .value_kind:     global_buffer
      - .actual_access:  read_only
        .address_space:  global
        .offset:         16
        .size:           8
        .value_kind:     global_buffer
      - .actual_access:  write_only
        .address_space:  global
        .offset:         24
        .size:           8
        .value_kind:     global_buffer
      - .actual_access:  write_only
        .address_space:  global
        .offset:         32
        .size:           8
        .value_kind:     global_buffer
    .group_segment_fixed_size: 116480
    .kernarg_segment_align: 8
    .kernarg_segment_size: 40
    .language:       OpenCL C
    .language_version:
      - 2
      - 0
    .max_flat_workgroup_size: 512
    .name:           _Z12conv3_kernelPK15HIP_vector_typeIjLj4EES2_PKfPfS5_
    .private_segment_fixed_size: 0
    .sgpr_count:     22
    .sgpr_spill_count: 0
    .symbol:         _Z12conv3_kernelPK15HIP_vector_typeIjLj4EES2_PKfPfS5_.kd
    .uniform_work_group_size: 1
    .uses_dynamic_stack: false
    .vgpr_count:     122
    .vgpr_spill_count: 0
    .wavefront_size: 64
  - .agpr_count:     0
    .args:
      - .actual_access:  read_only
        .address_space:  global
        .offset:         0
        .size:           8
        .value_kind:     global_buffer
      - .actual_access:  read_only
        .address_space:  global
        .offset:         8
        .size:           8
        .value_kind:     global_buffer
      - .actual_access:  write_only
        .address_space:  global
        .offset:         16
        .size:           8
        .value_kind:     global_buffer
      - .address_space:  global
        .offset:         24
        .size:           8
        .value_kind:     global_buffer
    .group_segment_fixed_size: 32768
    .kernarg_segment_align: 8
    .kernarg_segment_size: 32
    .language:       OpenCL C
    .language_version:
      - 2
      - 0
    .max_flat_workgroup_size: 256
    .name:           _Z15nms_hist_kernelPKfS0_PjS1_
    .private_segment_fixed_size: 0
    .sgpr_count:     102
    .sgpr_spill_count: 0
    .symbol:         _Z15nms_hist_kernelPKfS0_PjS1_.kd
    .uniform_work_group_size: 1
    .uses_dynamic_stack: false
    .vgpr_count:     128
    .vgpr_spill_count: 0
    .wavefront_size: 64
  - .agpr_count:     0
    .args:
      - .actual_access:  read_only
        .address_space:  global
        .offset:         0
        .size:           8
        .value_kind:     global_buffer
      - .actual_access:  write_only
        .address_space:  global
        .offset:         8
        .size:           8
        .value_kind:     global_buffer
    .group_segment_fixed_size: 4096
    .kernarg_segment_align: 8
    .kernarg_segment_size: 16
    .language:       OpenCL C
    .language_version:
      - 2
      - 0
    .max_flat_workgroup_size: 1024
    .name:           _Z17select_bin_kernelPKjPi
    .private_segment_fixed_size: 0
    .sgpr_count:     23
    .sgpr_spill_count: 0
    .symbol:         _Z17select_bin_kernelPKjPi.kd
    .uniform_work_group_size: 1
    .uses_dynamic_stack: false
    .vgpr_count:     13
    .vgpr_spill_count: 0
    .wavefront_size: 64
  - .agpr_count:     0
    .args:
      - .actual_access:  read_only
        .address_space:  global
        .offset:         0
        .size:           8
        .value_kind:     global_buffer
      - .actual_access:  read_only
        .address_space:  global
        .offset:         8
        .size:           8
        .value_kind:     global_buffer
      - .address_space:  global
        .offset:         16
        .size:           8
        .value_kind:     global_buffer
      - .actual_access:  write_only
        .address_space:  global
        .offset:         24
        .size:           8
        .value_kind:     global_buffer
    .group_segment_fixed_size: 2052
    .kernarg_segment_align: 8
    .kernarg_segment_size: 32
    .language:       OpenCL C
    .language_version:
      - 2
      - 0
    .max_flat_workgroup_size: 512
    .name:           _Z14collect_kernelPKjS0_PiS1_
    .private_segment_fixed_size: 0
    .sgpr_count:     54
    .sgpr_spill_count: 0
    .symbol:         _Z14collect_kernelPKjS0_PiS1_.kd
    .uniform_work_group_size: 1
    .uses_dynamic_stack: false
    .vgpr_count:     34
    .vgpr_spill_count: 0
    .wavefront_size: 64
  - .agpr_count:     0
    .args:
      - .actual_access:  read_only
        .address_space:  global
        .offset:         0
        .size:           8
        .value_kind:     global_buffer
      - .actual_access:  read_only
        .address_space:  global
        .offset:         8
        .size:           8
        .value_kind:     global_buffer
      - .actual_access:  read_only
        .address_space:  global
        .offset:         16
        .size:           8
        .value_kind:     global_buffer
      - .actual_access:  read_only
        .address_space:  global
        .offset:         24
        .size:           8
        .value_kind:     global_buffer
      - .actual_access:  write_only
        .address_space:  global
        .offset:         32
        .size:           8
        .value_kind:     global_buffer
    .group_segment_fixed_size: 49664
    .kernarg_segment_align: 8
    .kernarg_segment_size: 40
    .language:       OpenCL C
    .language_version:
      - 2
      - 0
    .max_flat_workgroup_size: 1024
    .name:           _Z11rank_kernelPKfS0_PKiS2_Pi
    .private_segment_fixed_size: 0
    .sgpr_count:     23
    .sgpr_spill_count: 0
    .symbol:         _Z11rank_kernelPKfS0_PKiS2_Pi.kd
    .uniform_work_group_size: 1
    .uses_dynamic_stack: false
    .vgpr_count:     12
    .vgpr_spill_count: 0
    .wavefront_size: 64
  - .agpr_count:     0
    .args:
      - .actual_access:  read_only
        .address_space:  global
        .offset:         0
        .size:           8
        .value_kind:     global_buffer
      - .actual_access:  read_only
        .address_space:  global
        .offset:         8
        .size:           8
        .value_kind:     global_buffer
      - .actual_access:  write_only
        .address_space:  global
        .offset:         16
        .size:           8
        .value_kind:     global_buffer
      - .actual_access:  write_only
        .address_space:  global
        .offset:         24
        .size:           8
        .value_kind:     global_buffer
    .group_segment_fixed_size: 0
    .kernarg_segment_align: 8
    .kernarg_segment_size: 32
    .language:       OpenCL C
    .language_version:
      - 2
      - 0
    .max_flat_workgroup_size: 256
    .name:           _Z15prep_kvw_kernelPKfS0_PDF16_S1_
    .private_segment_fixed_size: 0
    .sgpr_count:     14
    .sgpr_spill_count: 0
    .symbol:         _Z15prep_kvw_kernelPKfS0_PDF16_S1_.kd
    .uniform_work_group_size: 1
    .uses_dynamic_stack: false
    .vgpr_count:     7
    .vgpr_spill_count: 0
    .wavefront_size: 64
  - .agpr_count:     0
    .args:
      - .actual_access:  read_only
        .address_space:  global
        .offset:         0
        .size:           8
        .value_kind:     global_buffer
      - .actual_access:  read_only
        .address_space:  global
        .offset:         8
        .size:           8
        .value_kind:     global_buffer
      - .actual_access:  read_only
        .address_space:  global
        .offset:         16
        .size:           8
        .value_kind:     global_buffer
      - .actual_access:  read_only
        .address_space:  global
        .offset:         24
        .size:           8
        .value_kind:     global_buffer
      - .actual_access:  write_only
        .address_space:  global
        .offset:         32
        .size:           8
        .value_kind:     global_buffer
    .group_segment_fixed_size: 67856
    .kernarg_segment_align: 8
    .kernarg_segment_size: 40
    .language:       OpenCL C
    .language_version:
      - 2
      - 0
    .max_flat_workgroup_size: 448
    .name:           _Z17cross_attn_kernelPKDF16_S0_S0_S0_Pf
    .private_segment_fixed_size: 0
    .sgpr_count:     26
    .sgpr_spill_count: 0
    .symbol:         _Z17cross_attn_kernelPKDF16_S0_S0_S0_Pf.kd
    .uniform_work_group_size: 1
    .uses_dynamic_stack: false
    .vgpr_count:     74
    .vgpr_spill_count: 0
    .wavefront_size: 64
  - .agpr_count:     0
    .args:
      - .offset:         0
        .size:           424
        .value_kind:     by_value
      - .offset:         424
        .size:           88
        .value_kind:     by_value
    .group_segment_fixed_size: 137216
    .kernarg_segment_align: 8
    .kernarg_segment_size: 512
    .language:       OpenCL C
    .language_version:
      - 2
      - 0
    .max_flat_workgroup_size: 512
    .name:           _Z12tailA_kernel5TailP3KvP
    .private_segment_fixed_size: 0
    .sgpr_count:     44
    .sgpr_spill_count: 0
    .symbol:         _Z12tailA_kernel5TailP3KvP.kd
    .uniform_work_group_size: 1
    .uses_dynamic_stack: false
    .vgpr_count:     184
    .vgpr_spill_count: 0
    .wavefront_size: 64
  - .agpr_count:     0
    .args:
      - .offset:         0
        .size:           424
        .value_kind:     by_value
      - .offset:         424
        .size:           88
        .value_kind:     by_value
    .group_segment_fixed_size: 146592
    .kernarg_segment_align: 8
    .kernarg_segment_size: 512
    .language:       OpenCL C
    .language_version:
      - 2
      - 0
    .max_flat_workgroup_size: 512
    .name:           _Z12tailB_kernel5TailP3KvP
    .private_segment_fixed_size: 0
    .sgpr_count:     44
    .sgpr_spill_count: 0
    .symbol:         _Z12tailB_kernel5TailP3KvP.kd
    .uniform_work_group_size: 1
    .uses_dynamic_stack: false
    .vgpr_count:     216
    .vgpr_spill_count: 0
    .wavefront_size: 64
  - .agpr_count:     0
    .args:
      - .offset:         0
        .size:           424
        .value_kind:     by_value
    .group_segment_fixed_size: 36896
    .kernarg_segment_align: 8
    .kernarg_segment_size: 424
    .language:       OpenCL C
    .language_version:
      - 2
      - 0
    .max_flat_workgroup_size: 512
    .name:           _Z12tailC_kernel5TailP
    .private_segment_fixed_size: 0
    .sgpr_count:     58
    .sgpr_spill_count: 0
    .symbol:         _Z12tailC_kernel5TailP.kd
    .uniform_work_group_size: 1
    .uses_dynamic_stack: false
    .vgpr_count:     113
    .vgpr_spill_count: 0
    .wavefront_size: 64
  - .agpr_count:     0
    .args:
      - .offset:         0
        .size:           344
        .value_kind:     by_value
    .group_segment_fixed_size: 0
    .kernarg_segment_align: 8
    .kernarg_segment_size: 344
    .language:       OpenCL C
    .language_version:
      - 2
      - 0
    .max_flat_workgroup_size: 256
    .name:           _Z15prep_all_kernel5PrepP
    .private_segment_fixed_size: 0
    .sgpr_count:     31
    .sgpr_spill_count: 0
    .symbol:         _Z15prep_all_kernel5PrepP.kd
    .uniform_work_group_size: 1
    .uses_dynamic_stack: false
    .vgpr_count:     39
    .vgpr_spill_count: 0
    .wavefront_size: 64
  - .agpr_count:     0
    .args:
      - .actual_access:  read_only
        .address_space:  global
        .offset:         0
        .size:           8
        .value_kind:     global_buffer
      - .actual_access:  read_only
        .address_space:  global
        .offset:         8
        .size:           8
        .value_kind:     global_buffer
      - .actual_access:  read_only
        .address_space:  global
        .offset:         16
        .size:           8
        .value_kind:     global_buffer
      - .actual_access:  read_only
        .address_space:  global
        .offset:         24
        .size:           8
        .value_kind:     global_buffer
      - .actual_access:  read_only
        .address_space:  global
        .offset:         32
        .size:           8
        .value_kind:     global_buffer
      - .actual_access:  write_only
        .address_space:  global
        .offset:         40
        .size:           8
        .value_kind:     global_buffer
      - .actual_access:  read_only
        .address_space:  global
        .offset:         48
        .size:           8
        .value_kind:     global_buffer
      - .actual_access:  read_only
        .address_space:  global
        .offset:         56
        .size:           8
        .value_kind:     global_buffer
    .group_segment_fixed_size: 130304
    .kernarg_segment_align: 8
    .kernarg_segment_size: 64
    .language:       OpenCL C
    .language_version:
      - 2
      - 0
    .max_flat_workgroup_size: 512
    .name:           _Z11conv_kernelILi8ELi128ELi0EEvPK15HIP_vector_typeIjLj4EES3_PKfS5_S5_PDF16_PfS7_
    .private_segment_fixed_size: 0
    .sgpr_count:     30
    .sgpr_spill_count: 0
    .symbol:         _Z11conv_kernelILi8ELi128ELi0EEvPK15HIP_vector_typeIjLj4EES3_PKfS5_S5_PDF16_PfS7_.kd
    .uniform_work_group_size: 1
    .uses_dynamic_stack: false
    .vgpr_count:     254
    .vgpr_spill_count: 0
    .wavefront_size: 64
